# stack10
# speedup vs baseline: 1.0063x; 1.0038x over previous
.LBB3_36:
	s_setprio 0
	s_waitcnt vmcnt(0)
	ds_read_u16 v62, v233
	s_waitcnt lgkmcnt(1)
	v_bfe_u32 v76, v231, 23, 8
	s_cmp_eq_u32 s34, 1
	v_max_u32_e32 v76, 11, v76
	s_cselect_b64 s[24:25], -1, 0
	v_lshlrev_b32_e32 v240, 23, v76
	v_cndmask_b32_e64 v76, 2.0, 1.0, s[24:25]
	s_lshl_b32 s8, s34, 16
	v_mul_f32_e32 v230, v76, v230
	s_and_b32 s67, s8, 0x10000
	v_sub_u32_e32 v164, 0x84000000, v240
	v_pk_fma_f32 v[182:183], v[230:231], v[182:183], v[212:213] op_sel_hi:[0,1,1] neg_lo:[0,0,1] neg_hi:[0,0,1]
	v_pk_fma_f32 v[184:185], v[230:231], v[184:185], v[210:211] op_sel_hi:[0,1,1] neg_lo:[0,0,1] neg_hi:[0,0,1]
	v_pk_fma_f32 v[186:187], v[230:231], v[186:187], v[208:209] op_sel_hi:[0,1,1] neg_lo:[0,0,1] neg_hi:[0,0,1]
	v_pk_fma_f32 v[188:189], v[230:231], v[188:189], v[206:207] op_sel_hi:[0,1,1] neg_lo:[0,0,1] neg_hi:[0,0,1]
	v_fma_mixlo_f16 v58, v182, v164, 0 op_sel_hi:[0,0,0]
	v_fma_mixlo_f16 v59, v184, v164, 0 op_sel_hi:[0,0,0]
	v_fma_mixlo_f16 v60, v186, v164, 0 op_sel_hi:[0,0,0]
	v_fma_mixlo_f16 v61, v188, v164, 0 op_sel_hi:[0,0,0]
	s_waitcnt lgkmcnt(0)
	v_lshl_add_u32 v62, v62, 4, s67
	v_fma_mixhi_f16 v58, v183, v164, 0 op_sel_hi:[0,0,0]
	v_fma_mixhi_f16 v59, v185, v164, 0 op_sel_hi:[0,0,0]
	v_fma_mixhi_f16 v60, v187, v164, 0 op_sel_hi:[0,0,0]
	v_fma_mixhi_f16 v61, v189, v164, 0 op_sel_hi:[0,0,0]
	ds_write_b128 v62, v[58:61]
	ds_read_u16 v62, v233 offset:1024
	v_pk_fma_f32 v[198:199], v[230:231], v[198:199], v[196:197] op_sel_hi:[0,1,1] neg_lo:[0,0,1] neg_hi:[0,0,1]
	v_pk_fma_f32 v[200:201], v[230:231], v[200:201], v[194:195] op_sel_hi:[0,1,1] neg_lo:[0,0,1] neg_hi:[0,0,1]
	v_pk_fma_f32 v[202:203], v[230:231], v[202:203], v[192:193] op_sel_hi:[0,1,1] neg_lo:[0,0,1] neg_hi:[0,0,1]
	v_pk_fma_f32 v[204:205], v[230:231], v[204:205], v[190:191] op_sel_hi:[0,1,1] neg_lo:[0,0,1] neg_hi:[0,0,1]
	v_fma_mixlo_f16 v58, v198, v164, 0 op_sel_hi:[0,0,0]
	v_fma_mixlo_f16 v59, v200, v164, 0 op_sel_hi:[0,0,0]
	v_fma_mixlo_f16 v60, v202, v164, 0 op_sel_hi:[0,0,0]
	v_fma_mixlo_f16 v61, v204, v164, 0 op_sel_hi:[0,0,0]
	s_waitcnt lgkmcnt(0)
	v_lshl_add_u32 v62, v62, 4, s67
	v_fma_mixhi_f16 v58, v199, v164, 0 op_sel_hi:[0,0,0]
	v_fma_mixhi_f16 v59, v201, v164, 0 op_sel_hi:[0,0,0]
	v_fma_mixhi_f16 v60, v203, v164, 0 op_sel_hi:[0,0,0]
	v_fma_mixhi_f16 v61, v205, v164, 0 op_sel_hi:[0,0,0]
	ds_write_b128 v62, v[58:61]
	ds_read_u16 v62, v233 offset:2048
	v_pk_fma_f32 v[214:215], v[230:231], v[214:215], v[180:181] op_sel_hi:[0,1,1] neg_lo:[0,0,1] neg_hi:[0,0,1]
	v_pk_fma_f32 v[216:217], v[230:231], v[216:217], v[178:179] op_sel_hi:[0,1,1] neg_lo:[0,0,1] neg_hi:[0,0,1]
	v_pk_fma_f32 v[218:219], v[230:231], v[218:219], v[176:177] op_sel_hi:[0,1,1] neg_lo:[0,0,1] neg_hi:[0,0,1]
	v_pk_fma_f32 v[220:221], v[230:231], v[220:221], v[174:175] op_sel_hi:[0,1,1] neg_lo:[0,0,1] neg_hi:[0,0,1]
	v_fma_mixlo_f16 v58, v214, v164, 0 op_sel_hi:[0,0,0]
	v_fma_mixlo_f16 v59, v216, v164, 0 op_sel_hi:[0,0,0]
	v_fma_mixlo_f16 v60, v218, v164, 0 op_sel_hi:[0,0,0]
	v_fma_mixlo_f16 v61, v220, v164, 0 op_sel_hi:[0,0,0]
	s_waitcnt lgkmcnt(0)
	v_lshl_add_u32 v62, v62, 4, s67
	v_fma_mixhi_f16 v58, v215, v164, 0 op_sel_hi:[0,0,0]
	v_fma_mixhi_f16 v59, v217, v164, 0 op_sel_hi:[0,0,0]
	v_fma_mixhi_f16 v60, v219, v164, 0 op_sel_hi:[0,0,0]
	v_fma_mixhi_f16 v61, v221, v164, 0 op_sel_hi:[0,0,0]
	ds_write_b128 v62, v[58:61]
	ds_read_u16 v62, v233 offset:3072
	v_pk_fma_f32 v[222:223], v[230:231], v[222:223], v[172:173] op_sel_hi:[0,1,1] neg_lo:[0,0,1] neg_hi:[0,0,1]
	v_pk_fma_f32 v[224:225], v[230:231], v[224:225], v[170:171] op_sel_hi:[0,1,1] neg_lo:[0,0,1] neg_hi:[0,0,1]
	v_pk_fma_f32 v[226:227], v[230:231], v[226:227], v[168:169] op_sel_hi:[0,1,1] neg_lo:[0,0,1] neg_hi:[0,0,1]
	v_pk_fma_f32 v[228:229], v[230:231], v[228:229], v[166:167] op_sel_hi:[0,1,1] neg_lo:[0,0,1] neg_hi:[0,0,1]
	v_fma_mixlo_f16 v58, v222, v164, 0 op_sel_hi:[0,0,0]
	v_fma_mixlo_f16 v59, v224, v164, 0 op_sel_hi:[0,0,0]
	v_fma_mixlo_f16 v60, v226, v164, 0 op_sel_hi:[0,0,0]
	v_fma_mixlo_f16 v61, v228, v164, 0 op_sel_hi:[0,0,0]
	s_waitcnt lgkmcnt(0)
	v_lshl_add_u32 v62, v62, 4, s67
	v_fma_mixhi_f16 v58, v223, v164, 0 op_sel_hi:[0,0,0]
	v_fma_mixhi_f16 v59, v225, v164, 0 op_sel_hi:[0,0,0]
	v_fma_mixhi_f16 v60, v227, v164, 0 op_sel_hi:[0,0,0]
	v_fma_mixhi_f16 v61, v229, v164, 0 op_sel_hi:[0,0,0]
	v_pk_mul_f32 v[206:207], v[38:39], v[74:75]
	v_pk_mul_f32 v[208:209], v[40:41], v[74:75]
	v_pk_mul_f32 v[210:211], v[34:35], v[74:75]
	v_pk_mul_f32 v[212:213], v[36:37], v[74:75]
	v_pk_mul_f32 v[190:191], v[46:47], v[74:75]
	v_pk_mul_f32 v[192:193], v[48:49], v[74:75]
	v_pk_mul_f32 v[194:195], v[42:43], v[74:75]
	v_pk_mul_f32 v[196:197], v[44:45], v[74:75]
	v_pk_mul_f32 v[174:175], v[54:55], v[74:75]
	v_pk_mul_f32 v[176:177], v[56:57], v[74:75]
	v_pk_mul_f32 v[178:179], v[50:51], v[74:75]
	v_pk_mul_f32 v[180:181], v[52:53], v[74:75]
	v_pk_mul_f32 v[166:167], v[124:125], v[74:75]
	v_pk_mul_f32 v[168:169], v[128:129], v[74:75]
	v_pk_mul_f32 v[170:171], v[126:127], v[74:75]
	v_pk_mul_f32 v[172:173], v[130:131], v[74:75]
	s_andn2_b64 vcc, exec, s[12:13]
	s_mov_b64 s[24:25], -1
	ds_write_b128 v62, v[58:61]
	global_load_dwordx4 v[58:61], v[114:115], off
	global_load_dwordx4 v[62:65], v[116:117], off
	global_load_dwordx4 v[66:69], v[118:119], off
	global_load_dwordx4 v[70:73], v[120:121], off
	s_cbranch_vccnz .LBB3_38
	s_mov_b64 s[24:25], 0

.LBB3_51:
	v_max3_f32 v74, |v182|, 0, |v183|
	v_max3_f32 v74, v74, |v184|, |v185|
	v_max3_f32 v74, v74, |v186|, |v187|
	v_max3_f32 v74, v74, |v188|, |v189|
	v_max3_f32 v74, v74, |v198|, |v199|
	v_max3_f32 v74, v74, |v200|, |v201|
	v_max3_f32 v74, v74, |v202|, |v203|
	v_max3_f32 v74, v74, |v204|, |v205|
	v_max3_f32 v74, v74, |v214|, |v215|
	v_max3_f32 v74, v74, |v216|, |v217|
	v_max3_f32 v74, v74, |v218|, |v219|
	v_max3_f32 v74, v74, |v220|, |v221|
	v_max3_f32 v74, v74, |v222|, |v223|
	v_max3_f32 v74, v74, |v224|, |v225|
	v_max3_f32 v74, v74, |v226|, |v227|
	s_waitcnt vmcnt(0)
	v_max3_f32 v74, v74, |v228|, |v229|
	ds_read_u16 v62, v233 offset:4096
	v_pk_fma_f32 v[66:67], v[230:231], v[206:207], v[162:163] neg_lo:[0,0,1] neg_hi:[0,0,1]
	v_pk_fma_f32 v[68:69], v[230:231], v[208:209], v[160:161] neg_lo:[0,0,1] neg_hi:[0,0,1]
	v_max3_f32 v58, v74, |v66|, |v67|
	v_pk_fma_f32 v[70:71], v[230:231], v[210:211], v[158:159] neg_lo:[0,0,1] neg_hi:[0,0,1]
	v_max3_f32 v58, v58, |v68|, |v69|
	v_pk_fma_f32 v[72:73], v[230:231], v[212:213], v[156:157] neg_lo:[0,0,1] neg_hi:[0,0,1]
	v_max3_f32 v58, v58, |v70|, |v71|
	v_max3_f32 v63, v58, |v72|, |v73|
	v_fma_mixlo_f16 v58, v66, v164, 0 op_sel_hi:[0,0,0]
	v_fma_mixlo_f16 v59, v68, v164, 0 op_sel_hi:[0,0,0]
	v_fma_mixlo_f16 v60, v70, v164, 0 op_sel_hi:[0,0,0]
	v_fma_mixlo_f16 v61, v72, v164, 0 op_sel_hi:[0,0,0]
	s_waitcnt lgkmcnt(0)
	v_lshl_add_u32 v62, v62, 4, s67
	v_fma_mixhi_f16 v58, v67, v164, 0 op_sel_hi:[0,0,0]
	v_fma_mixhi_f16 v59, v69, v164, 0 op_sel_hi:[0,0,0]
	v_fma_mixhi_f16 v60, v71, v164, 0 op_sel_hi:[0,0,0]
	v_fma_mixhi_f16 v61, v73, v164, 0 op_sel_hi:[0,0,0]
	ds_write_b128 v62, v[58:61]
	v_pk_fma_f32 v[74:75], v[230:231], v[190:191], v[146:147] neg_lo:[0,0,1] neg_hi:[0,0,1]
	ds_read_u16 v62, v233 offset:5120
	v_pk_fma_f32 v[76:77], v[230:231], v[192:193], v[144:145] neg_lo:[0,0,1] neg_hi:[0,0,1]
	v_max3_f32 v58, v63, |v74|, |v75|
	v_pk_fma_f32 v[78:79], v[230:231], v[194:195], v[142:143] neg_lo:[0,0,1] neg_hi:[0,0,1]
	v_max3_f32 v58, v58, |v76|, |v77|
	v_pk_fma_f32 v[80:81], v[230:231], v[196:197], v[140:141] neg_lo:[0,0,1] neg_hi:[0,0,1]
	v_max3_f32 v58, v58, |v78|, |v79|
	v_max3_f32 v63, v58, |v80|, |v81|
	v_fma_mixlo_f16 v58, v74, v164, 0 op_sel_hi:[0,0,0]
	v_fma_mixhi_f16 v58, v75, v164, 0 op_sel_hi:[0,0,0]
	v_fma_mixlo_f16 v59, v76, v164, 0 op_sel_hi:[0,0,0]
	v_fma_mixlo_f16 v60, v78, v164, 0 op_sel_hi:[0,0,0]
	v_fma_mixlo_f16 v61, v80, v164, 0 op_sel_hi:[0,0,0]
	s_waitcnt lgkmcnt(0)
	v_lshl_add_u32 v62, v62, 4, s67
	v_pk_fma_f32 v[82:83], v[230:231], v[174:175], v[138:139] neg_lo:[0,0,1] neg_hi:[0,0,1]
	v_fma_mixhi_f16 v59, v77, v164, 0 op_sel_hi:[0,0,0]
	v_fma_mixhi_f16 v60, v79, v164, 0 op_sel_hi:[0,0,0]
	v_fma_mixhi_f16 v61, v81, v164, 0 op_sel_hi:[0,0,0]
	ds_write_b128 v62, v[58:61]
	v_pk_fma_f32 v[84:85], v[230:231], v[176:177], v[136:137] neg_lo:[0,0,1] neg_hi:[0,0,1]
	v_max3_f32 v58, v63, |v82|, |v83|
	v_pk_fma_f32 v[86:87], v[230:231], v[178:179], v[134:135] neg_lo:[0,0,1] neg_hi:[0,0,1]
	v_max3_f32 v58, v58, |v84|, |v85|
	v_pk_fma_f32 v[88:89], v[230:231], v[180:181], v[132:133] neg_lo:[0,0,1] neg_hi:[0,0,1]
	v_max3_f32 v58, v58, |v86|, |v87|
	v_max3_f32 v92, v58, |v88|, |v89|
	v_pk_fma_f32 v[62:63], v[230:231], v[166:167], v[148:149] neg_lo:[0,0,1] neg_hi:[0,0,1]
	v_pk_fma_f32 v[64:65], v[230:231], v[168:169], v[150:151] neg_lo:[0,0,1] neg_hi:[0,0,1]
	v_max3_f32 v92, v92, |v62|, |v63|
	v_pk_fma_f32 v[58:59], v[230:231], v[170:171], v[152:153] neg_lo:[0,0,1] neg_hi:[0,0,1]
	v_max3_f32 v92, v92, |v64|, |v65|
	v_pk_fma_f32 v[60:61], v[230:231], v[172:173], v[154:155] neg_lo:[0,0,1] neg_hi:[0,0,1]
	v_max3_f32 v92, v92, |v58|, |v59|
	v_max3_f32 v93, v92, |v60|, |v61|
	ds_bpermute_b32 v95, v234, v93
	ds_read_u16 v94, v233 offset:6144
	v_fma_mixlo_f16 v90, v82, v164, 0 op_sel_hi:[0,0,0]
	s_waitcnt lgkmcnt(1)
	v_max_f32_e32 v95, v95, v95
	v_max_f32_e32 v95, v93, v95
	ds_bpermute_b32 v96, v235, v95
	v_fma_mixhi_f16 v90, v83, v164, 0 op_sel_hi:[0,0,0]
	v_fma_mixlo_f16 v91, v84, v164, 0 op_sel_hi:[0,0,0]
	s_waitcnt lgkmcnt(0)
	v_max_f32_e32 v96, v96, v96
	v_max_f32_e32 v95, v95, v96
	ds_bpermute_b32 v96, v236, v95
	v_fma_mixlo_f16 v92, v86, v164, 0 op_sel_hi:[0,0,0]
	v_fma_mixlo_f16 v93, v88, v164, 0 op_sel_hi:[0,0,0]
	v_lshl_add_u32 v94, v94, 4, s67
	v_fma_mixhi_f16 v91, v85, v164, 0 op_sel_hi:[0,0,0]
	v_fma_mixhi_f16 v92, v87, v164, 0 op_sel_hi:[0,0,0]
	v_fma_mixhi_f16 v93, v89, v164, 0 op_sel_hi:[0,0,0]
	ds_write_b128 v94, v[90:93]
	s_waitcnt lgkmcnt(1)
	v_max_f32_e32 v90, v96, v96
	v_max_f32_e32 v90, v95, v90
	ds_bpermute_b32 v91, v237, v90
	ds_read_u16 v97, v233 offset:7168
	s_waitcnt lgkmcnt(1)
	v_max_f32_e32 v91, v91, v91
	v_max_f32_e32 v90, v90, v91
	ds_bpermute_b32 v91, v238, v90
	v_fma_mixlo_f16 v92, v62, v164, 0 op_sel_hi:[0,0,0]
	v_fma_mixlo_f16 v93, v64, v164, 0 op_sel_hi:[0,0,0]
	v_fma_mixlo_f16 v94, v58, v164, 0 op_sel_hi:[0,0,0]
	s_waitcnt lgkmcnt(0)
	v_max_f32_e32 v91, v91, v91
	v_max_f32_e32 v90, v90, v91
	ds_bpermute_b32 v91, v239, v90
	v_fma_mixlo_f16 v95, v60, v164, 0 op_sel_hi:[0,0,0]
	v_lshl_add_u32 v96, v97, 4, s67
	v_fma_mixhi_f16 v92, v63, v164, 0 op_sel_hi:[0,0,0]
	v_fma_mixhi_f16 v93, v65, v164, 0 op_sel_hi:[0,0,0]
	v_fma_mixhi_f16 v94, v59, v164, 0 op_sel_hi:[0,0,0]
	v_fma_mixhi_f16 v95, v61, v164, 0 op_sel_hi:[0,0,0]
	ds_write_b128 v96, v[92:95]
	s_and_saveexec_b64 s[24:25], s[4:5]
	s_cbranch_execz .LBB3_56
	s_waitcnt lgkmcnt(1)
	v_max_f32_e32 v91, v91, v91
	v_max_f32_e32 v90, v90, v90
	s_mov_b64 s[26:27], exec
	v_max_f32_e32 v90, v90, v91
	s_mov_b32 s8, 0
